# cmp-attn importance stores: blocks 1-3 reuse block 0's LDS address with immediate offsets and compare against s23-4k (9 VALU fewer per pass-2 quad-tile)
# speedup vs baseline: 1.0050x; 1.0050x over previous
;     ...
;                             for (int kt = 0; kt < 4; ++kt) rot[kt] = __shfl(im3[kt], (lane + 48) & 63);
; #pragma unroll
;                             for (int kt = 0; kt < 4; ++kt) { const float pv3 = q > 0 ? rot[kt] : (kt == 0 ? carry3[qd] : rot[kt > 0 ? kt - 1 : 0]);
;                                 const int jg = (p0 + 16 * kt + 4 * q) >> 2;
;                                 if (hr == 0 && jg < 256) sscore[(tq - t0) * SSTR + jg] = base[kt] + pv3; }
;                             carry3[qd] = rot[3];
.LBB0_895:
	s_or_b64 exec, exec, s[4:5]
	s_add_i32 s14, s23, -4
	v_cmp_gt_i32_e32 vcc, s14, v127
	s_and_b64 s[14:15], s[2:3], vcc
	s_and_saveexec_b64 s[4:5], s[14:15]
	s_cbranch_execz .LBB0_897
	v_add_f32_e32 v123, v239, v245
	v_add_f32_e32 v123, v123, v247
	v_fmac_f32_e32 v241, 2.0, v123
	s_waitcnt lgkmcnt(2)
	v_cndmask_b32_e64 v123, v248, v192, s[0:1]
	v_add_f32_e32 v123, v241, v123
	ds_write_b32 v122, v123 offset:16400
.LBB0_897:
	s_or_b64 exec, exec, s[4:5]
	s_add_i32 s14, s23, -8
	v_cmp_gt_i32_e32 vcc, s14, v127
	s_and_b64 s[14:15], s[2:3], vcc
	s_and_saveexec_b64 s[4:5], s[14:15]
	s_cbranch_execz .LBB0_899
	v_add_f32_e32 v123, v136, v165
	v_add_f32_e32 v123, v123, v237
	v_fmac_f32_e32 v164, 2.0, v123
	s_waitcnt lgkmcnt(1)
	v_cndmask_b32_e64 v123, v134, v248, s[0:1]
	v_add_f32_e32 v123, v164, v123
	ds_write_b32 v122, v123 offset:16416
.LBB0_899:
	s_or_b64 exec, exec, s[4:5]
	s_add_i32 s14, s23, -12
	v_cmp_gt_i32_e32 vcc, s14, v127
	s_and_b64 s[14:15], s[2:3], vcc
	s_and_saveexec_b64 s[4:5], s[14:15]
	s_cbranch_execz .LBB0_901
	v_add_f32_e32 v123, v130, v133
	v_add_f32_e32 v123, v123, v236
	v_fmac_f32_e32 v132, 2.0, v123
	s_waitcnt lgkmcnt(0)
	v_cndmask_b32_e64 v123, v128, v134, s[0:1]
	v_add_f32_e32 v123, v132, v123
	ds_write_b32 v122, v123 offset:16432

;     ...
;                             for (int kt = 0; kt < 4; ++kt) rot[kt] = __shfl(im3[kt], (lane + 48) & 63);
; #pragma unroll
;                             for (int kt = 0; kt < 4; ++kt) { const float pv3 = q > 0 ? rot[kt] : (kt == 0 ? carry3[qd] : rot[kt > 0 ? kt - 1 : 0]);
;                                 const int jg = (p0 + 16 * kt + 4 * q) >> 2;
;                                 if (hr == 0 && jg < 256) sscore[(tq - t0) * SSTR + jg] = base[kt] + pv3; }
;                             carry3[qd] = rot[3];
.LBB0_911:
	s_or_b64 exec, exec, s[4:5]
	s_add_i32 s14, s23, -4
	v_cmp_gt_i32_e32 vcc, s14, v127
	s_and_b64 s[14:15], s[2:3], vcc
	s_and_saveexec_b64 s[4:5], s[14:15]
	s_cbranch_execz .LBB0_913
	v_add_f32_e32 v91, v111, v114
	v_add_f32_e32 v91, v91, v116
	v_fmac_f32_e32 v113, 2.0, v91
	s_waitcnt lgkmcnt(2)
	v_cndmask_b32_e64 v91, v117, v121, s[0:1]
	v_add_f32_e32 v91, v113, v91
	ds_write_b32 v90, v91 offset:16400
.LBB0_913:
	s_or_b64 exec, exec, s[4:5]
	s_add_i32 s14, s23, -8
	v_cmp_gt_i32_e32 vcc, s14, v127
	s_and_b64 s[14:15], s[2:3], vcc
	s_and_saveexec_b64 s[4:5], s[14:15]
	s_cbranch_execz .LBB0_915
	v_add_f32_e32 v91, v103, v106
	v_add_f32_e32 v91, v91, v109
	v_fmac_f32_e32 v105, 2.0, v91
	s_waitcnt lgkmcnt(1)
	v_cndmask_b32_e64 v91, v101, v117, s[0:1]
	v_add_f32_e32 v91, v105, v91
	ds_write_b32 v90, v91 offset:16416
.LBB0_915:
	s_or_b64 exec, exec, s[4:5]
	s_add_i32 s14, s23, -12
	v_cmp_gt_i32_e32 vcc, s14, v127
	s_and_b64 s[14:15], s[2:3], vcc
	s_and_saveexec_b64 s[4:5], s[14:15]
	s_cbranch_execz .LBB0_917
	v_add_f32_e32 v91, v96, v99
	v_add_f32_e32 v91, v91, v107
	v_fmac_f32_e32 v98, 2.0, v91
	s_waitcnt lgkmcnt(0)
	v_cndmask_b32_e64 v91, v94, v101, s[0:1]
	v_add_f32_e32 v91, v98, v91
	ds_write_b32 v90, v91 offset:16432
